# prologue de-serialisation: 16 per-item gain loads of weight conversion batched into distinct VGPRs (6 code paths)
# baseline (speedup 1.0000x reference)
.LBB0_80:
	s_andn2_b64 vcc, exec, s[8:9]
	s_cbranch_vccnz .LBB0_82
	v_readlane_b32 s68, v253, 9
	v_readlane_b32 s69, v253, 10
	s_add_u32 s68, s68, s11
	s_addc_u32 s69, s69, 0
	s_mul_i32 s8, s10, 0x1800000
	s_add_u32 s12, s22, s8
	s_mul_i32 s8, s0, 0x2aab
	s_addc_u32 s13, s23, 0
	s_lshr_b32 s9, s8, 31
	s_ashr_i32 s8, s8, 19
	s_add_i32 s8, s8, s9
	s_mul_i32 s15, s8, 0xffffffd0
	s_add_i32 s15, s15, s0
	s_lshl_b32 s14, s8, 6
	s_lshl_b32 s8, s15, 6
	v_add_u32_e32 v74, s14, v77
	v_mov_b64_e32 v[0:1], s[68:69]
	s_movk_i32 s1, 0x3000
	v_mad_i64_i32 v[0:1], s[68:69], v74, s1, v[0:1]
	s_ashr_i32 s9, s8, 31
	v_readlane_b32 s2, v254, 48
	v_ashrrev_i32_e32 v75, 31, v74
	v_lshl_add_u64 v[0:1], s[8:9], 2, v[0:1]
	v_readlane_b32 s3, v254, 49
	v_lshl_add_u64 v[0:1], v[0:1], 0, v[64:65]
	global_load_dwordx4 v[4:7], v[0:1], off
	v_lshl_add_u64 v[74:75], v[74:75], 2, s[2:3]
	global_load_dword v116, v[74:75], off
	global_load_dword v118, v[74:75], off offset:16
	global_load_dword v120, v[74:75], off offset:32
	global_load_dword v122, v[74:75], off offset:48
	global_load_dword v124, v[74:75], off offset:64
	global_load_dword v126, v[74:75], off offset:80
	global_load_dword v128, v[74:75], off offset:96
	global_load_dword v130, v[74:75], off offset:112
	global_load_dword v132, v[74:75], off offset:128
	global_load_dword v134, v[74:75], off offset:144
	global_load_dword v136, v[74:75], off offset:160
	global_load_dword v138, v[74:75], off offset:176
	global_load_dword v140, v[74:75], off offset:192
	global_load_dword v142, v[74:75], off offset:208
	global_load_dword v144, v[74:75], off offset:224
	global_load_dword v146, v[74:75], off offset:240
	v_add_co_u32_e32 v2, vcc, s81, v0
	s_mov_b32 s1, 0x54000
	s_nop 0
	v_addc_co_u32_e32 v3, vcc, 0, v1, vcc
	global_load_dwordx4 v[8:11], v[2:3], off
	v_add_co_u32_e32 v2, vcc, s82, v0
	s_lshl_b32 s9, s15, 7
	s_nop 0
	v_addc_co_u32_e32 v3, vcc, 0, v1, vcc
	global_load_dwordx4 v[12:15], v[2:3], off
	v_add_co_u32_e32 v2, vcc, s85, v0
	s_and_b32 s8, s8, 64
	s_nop 0
	v_addc_co_u32_e32 v3, vcc, 0, v1, vcc
	global_load_dwordx4 v[16:19], v[2:3], off
	v_add_co_u32_e32 v2, vcc, s34, v0
	s_or_b32 s8, s8, s9
	s_nop 0
	v_addc_co_u32_e32 v3, vcc, 0, v1, vcc
	global_load_dwordx4 v[20:23], v[2:3], off
	v_add_co_u32_e32 v2, vcc, s88, v0
	s_bitset1_b32 s8, 7
	s_nop 0
	v_addc_co_u32_e32 v3, vcc, 0, v1, vcc
	global_load_dwordx4 v[24:27], v[2:3], off
	v_add_co_u32_e32 v2, vcc, s86, v0
	s_ashr_i32 s9, s14, 31
	s_nop 0
	v_addc_co_u32_e32 v3, vcc, 0, v1, vcc
	global_load_dwordx4 v[28:31], v[2:3], off
	v_add_co_u32_e32 v2, vcc, s1, v0
	s_mov_b32 s1, 0x6c000
	s_nop 0
	v_addc_co_u32_e32 v3, vcc, 0, v1, vcc
	global_load_dwordx4 v[32:35], v[2:3], off
	v_add_co_u32_e32 v2, vcc, s53, v0
	s_add_u32 s12, s12, s14
	s_nop 0
	v_addc_co_u32_e32 v3, vcc, 0, v1, vcc
	global_load_dwordx4 v[36:39], v[2:3], off
	v_add_co_u32_e32 v2, vcc, s1, v0
	s_mov_b32 s1, 0x84000
	s_nop 0
	v_addc_co_u32_e32 v3, vcc, 0, v1, vcc
	global_load_dwordx4 v[44:47], v[2:3], off
	v_add_co_u32_e32 v2, vcc, s89, v0
	s_addc_u32 s13, s13, s9
	s_nop 0
	v_addc_co_u32_e32 v3, vcc, 0, v1, vcc
	global_load_dwordx4 v[52:55], v[2:3], off
	v_add_co_u32_e32 v2, vcc, s1, v0
	s_mov_b32 s1, 0x9c000
	s_nop 0
	v_addc_co_u32_e32 v3, vcc, 0, v1, vcc
	global_load_dwordx4 v[60:63], v[2:3], off
	v_add_co_u32_e32 v2, vcc, s95, v0
	v_readlane_b32 s70, v253, 11
	s_nop 0
	v_addc_co_u32_e32 v3, vcc, 0, v1, vcc
	global_load_dwordx4 v[56:59], v[2:3], off
	v_add_co_u32_e32 v2, vcc, s1, v0
	s_mov_b32 s1, 0xb4000
	s_nop 0
	v_addc_co_u32_e32 v3, vcc, 0, v1, vcc
	global_load_dwordx4 v[48:51], v[2:3], off
	v_add_co_u32_e32 v2, vcc, s80, v0
	v_addc_co_u32_e32 v3, vcc, 0, v1, vcc
	v_add_co_u32_e32 v0, vcc, s1, v0
	global_load_dwordx4 v[40:43], v[2:3], off
	s_nop 0
	v_addc_co_u32_e32 v1, vcc, 0, v1, vcc
	global_load_dwordx4 v[0:3], v[0:1], off
	v_readlane_b32 s71, v253, 12
	v_readlane_b32 s72, v253, 13
	v_readlane_b32 s73, v253, 14
	v_readlane_b32 s74, v253, 15
	v_readlane_b32 s75, v253, 16
	s_waitcnt vmcnt(0)
	v_pk_mul_f32 v[4:5], v[4:5], v[116:117] op_sel_hi:[1,0]
	v_pk_mul_f32 v[6:7], v[6:7], v[116:117] op_sel_hi:[1,0]
	v_pk_mul_f32 v[10:11], v[10:11], v[118:119] op_sel_hi:[1,0]
	v_pk_mul_f32 v[8:9], v[8:9], v[118:119] op_sel_hi:[1,0]
	v_pk_mul_f32 v[14:15], v[14:15], v[120:121] op_sel_hi:[1,0]
	v_pk_mul_f32 v[12:13], v[12:13], v[120:121] op_sel_hi:[1,0]
	v_pk_mul_f32 v[18:19], v[18:19], v[122:123] op_sel_hi:[1,0]
	v_pk_mul_f32 v[16:17], v[16:17], v[122:123] op_sel_hi:[1,0]
	v_pk_mul_f32 v[22:23], v[22:23], v[124:125] op_sel_hi:[1,0]
	v_pk_mul_f32 v[20:21], v[20:21], v[124:125] op_sel_hi:[1,0]
	v_pk_mul_f32 v[26:27], v[26:27], v[126:127] op_sel_hi:[1,0]
	v_pk_mul_f32 v[24:25], v[24:25], v[126:127] op_sel_hi:[1,0]
	v_pk_mul_f32 v[30:31], v[30:31], v[128:129] op_sel_hi:[1,0]
	v_pk_mul_f32 v[28:29], v[28:29], v[128:129] op_sel_hi:[1,0]
	v_pk_mul_f32 v[34:35], v[34:35], v[130:131] op_sel_hi:[1,0]
	v_pk_mul_f32 v[32:33], v[32:33], v[130:131] op_sel_hi:[1,0]
	v_pk_mul_f32 v[38:39], v[38:39], v[132:133] op_sel_hi:[1,0]
	v_pk_mul_f32 v[36:37], v[36:37], v[132:133] op_sel_hi:[1,0]
	v_pk_mul_f32 v[46:47], v[46:47], v[134:135] op_sel_hi:[1,0]
	v_pk_mul_f32 v[44:45], v[44:45], v[134:135] op_sel_hi:[1,0]
	v_pk_mul_f32 v[54:55], v[54:55], v[136:137] op_sel_hi:[1,0]
	v_pk_mul_f32 v[52:53], v[52:53], v[136:137] op_sel_hi:[1,0]
	v_pk_mul_f32 v[62:63], v[62:63], v[138:139] op_sel_hi:[1,0]
	v_pk_mul_f32 v[60:61], v[60:61], v[138:139] op_sel_hi:[1,0]
	v_pk_mul_f32 v[58:59], v[58:59], v[140:141] op_sel_hi:[1,0]
	v_pk_mul_f32 v[56:57], v[56:57], v[140:141] op_sel_hi:[1,0]
	v_pk_mul_f32 v[50:51], v[50:51], v[142:143] op_sel_hi:[1,0]
	v_pk_mul_f32 v[48:49], v[48:49], v[142:143] op_sel_hi:[1,0]
	v_pk_mul_f32 v[42:43], v[42:43], v[144:145] op_sel_hi:[1,0]
	v_pk_mul_f32 v[40:41], v[40:41], v[144:145] op_sel_hi:[1,0]
	v_pk_mul_f32 v[2:3], v[2:3], v[146:147] op_sel_hi:[1,0]
	v_pk_mul_f32 v[0:1], v[0:1], v[146:147] op_sel_hi:[1,0]
	ds_write_b128 v78, v[4:7]
	ds_write_b128 v78, v[8:11] offset:1088
	ds_write_b128 v78, v[12:15] offset:2176
	ds_write_b128 v78, v[16:19] offset:3264
	ds_write_b128 v79, v[20:23] offset:4352
	ds_write_b128 v79, v[24:27] offset:5440
	ds_write_b128 v79, v[28:31] offset:6528
	ds_write_b128 v79, v[32:35] offset:7616
	ds_write_b128 v80, v[36:39] offset:8704
	ds_write_b128 v80, v[44:47] offset:9792
	ds_write_b128 v80, v[52:55] offset:10880
	ds_write_b128 v80, v[60:63] offset:11968
	ds_write_b128 v81, v[56:59] offset:13056
	ds_write_b128 v81, v[48:51] offset:14144
	ds_write_b128 v81, v[40:43] offset:15232
	ds_write_b128 v81, v[0:3] offset:16320
	s_waitcnt lgkmcnt(0)
	ds_read2_b32 v[2:3], v83 offset1:68
	v_lshl_add_u64 v[0:1], s[12:13], 0, v[66:67]
	s_waitcnt lgkmcnt(0)
	v_mul_f32_e32 v4, 0x42800000, v2
	v_mul_f32_e32 v5, 0x42800000, v3
	ds_read2_b32 v[2:3], v83 offset0:136 offset1:204
	s_waitcnt lgkmcnt(0)
	v_mul_f32_e32 v6, 0x42800000, v2
	v_mov_b32_e32 v2, v65
	v_cvt_pk_fp8_f32 v2, v4, v5
	ds_read2_b32 v[4:5], v110 offset0:16 offset1:84
	v_mul_f32_e32 v3, 0x42800000, v3
	v_cvt_pk_fp8_f32 v2, v6, v3 op_sel:[0,0,1]
	v_mov_b32_e32 v3, v65
	s_waitcnt lgkmcnt(0)
	v_mul_f32_e32 v6, 0x42800000, v4
	v_mul_f32_e32 v7, 0x42800000, v5
	ds_read2_b32 v[4:5], v110 offset0:152 offset1:220
	v_cvt_pk_fp8_f32 v3, v6, v7
	v_add_u32_e32 v6, 0x800, v83
	s_waitcnt lgkmcnt(0)
	v_mul_f32_e32 v4, 0x42800000, v4
	v_mul_f32_e32 v5, 0x42800000, v5
	v_cvt_pk_fp8_f32 v3, v4, v5 op_sel:[0,0,1]
	ds_read2_b32 v[4:5], v6 offset0:32 offset1:100
	s_waitcnt lgkmcnt(0)
	v_mul_f32_e32 v7, 0x42800000, v4
	v_mul_f32_e32 v8, 0x42800000, v5
	ds_read2_b32 v[4:5], v6 offset0:168 offset1:236
	s_waitcnt lgkmcnt(0)
	v_mul_f32_e32 v6, 0x42800000, v4
	v_mov_b32_e32 v4, v65
	v_cvt_pk_fp8_f32 v4, v7, v8
	v_mul_f32_e32 v5, 0x42800000, v5
	v_cvt_pk_fp8_f32 v4, v6, v5 op_sel:[0,0,1]
	v_add_u32_e32 v5, 0xc00, v83
	ds_read2_b32 v[6:7], v5 offset0:48 offset1:116
	s_waitcnt lgkmcnt(0)
	v_mul_f32_e32 v8, 0x42800000, v6
	v_mul_f32_e32 v9, 0x42800000, v7
	ds_read2_b32 v[6:7], v5 offset0:184 offset1:252
	v_mov_b32_e32 v5, v65
	v_cvt_pk_fp8_f32 v5, v8, v9
	s_waitcnt lgkmcnt(0)
	v_mul_f32_e32 v6, 0x42800000, v6
	v_mul_f32_e32 v7, 0x42800000, v7
	v_cvt_pk_fp8_f32 v5, v6, v7 op_sel:[0,0,1]
	v_add_u32_e32 v6, s8, v82
	v_ashrrev_i32_e32 v7, 31, v6
	v_lshlrev_b64 v[6:7], 12, v[6:7]
	v_lshl_add_u64 v[6:7], v[0:1], 0, v[6:7]
	global_store_dwordx4 v[6:7], v[2:5], off
	ds_read2_b32 v[2:3], v85 offset1:68
	s_waitcnt lgkmcnt(0)
	v_mul_f32_e32 v4, 0x42800000, v2
	v_mul_f32_e32 v5, 0x42800000, v3
	ds_read2_b32 v[2:3], v85 offset0:136 offset1:204
	s_waitcnt lgkmcnt(0)
	v_mul_f32_e32 v6, 0x42800000, v2
	v_mov_b32_e32 v2, v65
	v_cvt_pk_fp8_f32 v2, v4, v5
	v_mul_f32_e32 v3, 0x42800000, v3
	v_cvt_pk_fp8_f32 v2, v6, v3 op_sel:[0,0,1]
	v_add_u32_e32 v3, 0x400, v85
	ds_read2_b32 v[4:5], v3 offset0:16 offset1:84
	s_waitcnt lgkmcnt(0)
	v_mul_f32_e32 v6, 0x42800000, v4
	v_mul_f32_e32 v7, 0x42800000, v5
	ds_read2_b32 v[4:5], v3 offset0:152 offset1:220
	v_mov_b32_e32 v3, v65
	v_cvt_pk_fp8_f32 v3, v6, v7
	v_add_u32_e32 v6, 0x800, v85
	s_waitcnt lgkmcnt(0)
	v_mul_f32_e32 v4, 0x42800000, v4
	v_mul_f32_e32 v5, 0x42800000, v5
	v_cvt_pk_fp8_f32 v3, v4, v5 op_sel:[0,0,1]
	ds_read2_b32 v[4:5], v6 offset0:32 offset1:100
	s_waitcnt lgkmcnt(0)
	v_mul_f32_e32 v7, 0x42800000, v4
	v_mul_f32_e32 v8, 0x42800000, v5
	ds_read2_b32 v[4:5], v6 offset0:168 offset1:236
	s_waitcnt lgkmcnt(0)
	v_mul_f32_e32 v6, 0x42800000, v4
	v_mov_b32_e32 v4, v65
	v_cvt_pk_fp8_f32 v4, v7, v8
	v_mul_f32_e32 v5, 0x42800000, v5
	v_cvt_pk_fp8_f32 v4, v6, v5 op_sel:[0,0,1]
	v_add_u32_e32 v5, 0xc00, v85
	ds_read2_b32 v[6:7], v5 offset0:48 offset1:116
	s_waitcnt lgkmcnt(0)
	v_mul_f32_e32 v8, 0x42800000, v6
	v_mul_f32_e32 v9, 0x42800000, v7
	ds_read2_b32 v[6:7], v5 offset0:184 offset1:252
	v_mov_b32_e32 v5, v65
	v_cvt_pk_fp8_f32 v5, v8, v9
	s_waitcnt lgkmcnt(0)
	v_mul_f32_e32 v6, 0x42800000, v6
	v_mul_f32_e32 v7, 0x42800000, v7
	v_cvt_pk_fp8_f32 v5, v6, v7 op_sel:[0,0,1]
	v_add_u32_e32 v6, s8, v84
	v_ashrrev_i32_e32 v7, 31, v6
	v_lshlrev_b64 v[6:7], 12, v[6:7]
	v_lshl_add_u64 v[6:7], v[0:1], 0, v[6:7]
	global_store_dwordx4 v[6:7], v[2:5], off
	ds_read2_b32 v[2:3], v87 offset1:68
	s_waitcnt lgkmcnt(0)
	v_mul_f32_e32 v4, 0x42800000, v2
	v_mul_f32_e32 v5, 0x42800000, v3
	ds_read2_b32 v[2:3], v87 offset0:136 offset1:204
	s_waitcnt lgkmcnt(0)
	v_mul_f32_e32 v6, 0x42800000, v2
	v_mov_b32_e32 v2, v65
	v_cvt_pk_fp8_f32 v2, v4, v5
	v_mul_f32_e32 v3, 0x42800000, v3
	v_cvt_pk_fp8_f32 v2, v6, v3 op_sel:[0,0,1]
	v_add_u32_e32 v3, 0x400, v87
	ds_read2_b32 v[4:5], v3 offset0:16 offset1:84
	s_waitcnt lgkmcnt(0)
	v_mul_f32_e32 v6, 0x42800000, v4
	v_mul_f32_e32 v7, 0x42800000, v5
	ds_read2_b32 v[4:5], v3 offset0:152 offset1:220
	v_mov_b32_e32 v3, v65
	v_cvt_pk_fp8_f32 v3, v6, v7
	v_add_u32_e32 v6, 0x800, v87
	s_waitcnt lgkmcnt(0)
	v_mul_f32_e32 v4, 0x42800000, v4
	v_mul_f32_e32 v5, 0x42800000, v5
	v_cvt_pk_fp8_f32 v3, v4, v5 op_sel:[0,0,1]
	ds_read2_b32 v[4:5], v6 offset0:32 offset1:100
	s_waitcnt lgkmcnt(0)
	v_mul_f32_e32 v7, 0x42800000, v4
	v_mul_f32_e32 v8, 0x42800000, v5
	ds_read2_b32 v[4:5], v6 offset0:168 offset1:236
	s_waitcnt lgkmcnt(0)
	v_mul_f32_e32 v6, 0x42800000, v4
	v_mov_b32_e32 v4, v65
	v_cvt_pk_fp8_f32 v4, v7, v8
	v_mul_f32_e32 v5, 0x42800000, v5
	v_cvt_pk_fp8_f32 v4, v6, v5 op_sel:[0,0,1]
	v_add_u32_e32 v5, 0xc00, v87
	ds_read2_b32 v[6:7], v5 offset0:48 offset1:116
	s_waitcnt lgkmcnt(0)
	v_mul_f32_e32 v8, 0x42800000, v6
	v_mul_f32_e32 v9, 0x42800000, v7
	ds_read2_b32 v[6:7], v5 offset0:184 offset1:252
	v_mov_b32_e32 v5, v65
	v_cvt_pk_fp8_f32 v5, v8, v9
	s_waitcnt lgkmcnt(0)
	v_mul_f32_e32 v6, 0x42800000, v6
	v_mul_f32_e32 v7, 0x42800000, v7
	v_cvt_pk_fp8_f32 v5, v6, v7 op_sel:[0,0,1]
	v_add_u32_e32 v6, s8, v86
	v_ashrrev_i32_e32 v7, 31, v6
	v_lshlrev_b64 v[6:7], 12, v[6:7]
	v_lshl_add_u64 v[6:7], v[0:1], 0, v[6:7]
	global_store_dwordx4 v[6:7], v[2:5], off
	ds_read2_b32 v[2:3], v89 offset1:68
	s_waitcnt lgkmcnt(0)
	v_mul_f32_e32 v4, 0x42800000, v2
	v_mul_f32_e32 v5, 0x42800000, v3
	ds_read2_b32 v[2:3], v89 offset0:136 offset1:204
	s_waitcnt lgkmcnt(0)
	v_mul_f32_e32 v6, 0x42800000, v2
	v_mov_b32_e32 v2, v65
	v_cvt_pk_fp8_f32 v2, v4, v5
	v_mul_f32_e32 v3, 0x42800000, v3
	v_cvt_pk_fp8_f32 v2, v6, v3 op_sel:[0,0,1]
	v_add_u32_e32 v3, 0x400, v89
	ds_read2_b32 v[4:5], v3 offset0:16 offset1:84
	s_waitcnt lgkmcnt(0)
	v_mul_f32_e32 v6, 0x42800000, v4
	v_mul_f32_e32 v7, 0x42800000, v5
	ds_read2_b32 v[4:5], v3 offset0:152 offset1:220
	v_mov_b32_e32 v3, v65
	v_cvt_pk_fp8_f32 v3, v6, v7
	v_add_u32_e32 v6, 0x800, v89
	s_waitcnt lgkmcnt(0)
	v_mul_f32_e32 v4, 0x42800000, v4
	v_mul_f32_e32 v5, 0x42800000, v5
	v_cvt_pk_fp8_f32 v3, v4, v5 op_sel:[0,0,1]
	ds_read2_b32 v[4:5], v6 offset0:32 offset1:100
	s_waitcnt lgkmcnt(0)
	v_mul_f32_e32 v7, 0x42800000, v4
	v_mul_f32_e32 v8, 0x42800000, v5
	ds_read2_b32 v[4:5], v6 offset0:168 offset1:236
	s_waitcnt lgkmcnt(0)
	v_mul_f32_e32 v6, 0x42800000, v4
	v_mov_b32_e32 v4, v65
	v_cvt_pk_fp8_f32 v4, v7, v8
	v_mul_f32_e32 v5, 0x42800000, v5
	v_cvt_pk_fp8_f32 v4, v6, v5 op_sel:[0,0,1]
	v_add_u32_e32 v5, 0xc00, v89
	ds_read2_b32 v[6:7], v5 offset0:48 offset1:116
	s_waitcnt lgkmcnt(0)
	v_mul_f32_e32 v8, 0x42800000, v6
	v_mul_f32_e32 v9, 0x42800000, v7
	ds_read2_b32 v[6:7], v5 offset0:184 offset1:252
	v_mov_b32_e32 v5, v65
	v_cvt_pk_fp8_f32 v5, v8, v9
	s_waitcnt lgkmcnt(0)
	v_mul_f32_e32 v6, 0x42800000, v6
	v_mul_f32_e32 v7, 0x42800000, v7
	v_cvt_pk_fp8_f32 v5, v6, v7 op_sel:[0,0,1]
	v_add_u32_e32 v6, s8, v88
	v_ashrrev_i32_e32 v7, 31, v6
	v_lshlrev_b64 v[6:7], 12, v[6:7]
	v_lshl_add_u64 v[0:1], v[0:1], 0, v[6:7]
	global_store_dwordx4 v[0:1], v[2:5], off
	s_waitcnt lgkmcnt(0)

.LBB0_83:
	s_andn2_b64 vcc, exec, s[8:9]
	s_cbranch_vccnz .LBB0_85
	v_readlane_b32 s36, v254, 3
	v_readlane_b32 s50, v254, 17
	v_readlane_b32 s51, v254, 18
	s_add_u32 s14, s50, s11
	s_addc_u32 s15, s51, 0
	s_mul_i32 s10, s10, 0x1800000
	s_add_u32 s10, s22, s10
	s_mul_i32 s8, s0, 0x2aab
	s_addc_u32 s11, s23, 0
	s_lshr_b32 s9, s8, 31
	s_ashr_i32 s8, s8, 19
	s_add_i32 s8, s8, s9
	s_mul_i32 s9, s8, 0xffffffd0
	s_add_i32 s0, s9, s0
	s_lshl_b32 s12, s8, 6
	s_lshl_b32 s8, s0, 6
	v_add_u32_e32 v74, s12, v77
	v_mov_b64_e32 v[0:1], s[14:15]
	s_movk_i32 s1, 0x3000
	v_mad_i64_i32 v[0:1], s[14:15], v74, s1, v[0:1]
	s_ashr_i32 s9, s8, 31
	v_readlane_b32 s2, v254, 48
	v_ashrrev_i32_e32 v75, 31, v74
	v_lshl_add_u64 v[0:1], s[8:9], 2, v[0:1]
	v_readlane_b32 s3, v254, 49
	v_lshl_add_u64 v[0:1], v[0:1], 0, v[64:65]
	global_load_dwordx4 v[4:7], v[0:1], off
	v_lshl_add_u64 v[74:75], v[74:75], 2, s[2:3]
	global_load_dword v116, v[74:75], off
	global_load_dword v118, v[74:75], off offset:16
	global_load_dword v120, v[74:75], off offset:32
	global_load_dword v122, v[74:75], off offset:48
	global_load_dword v124, v[74:75], off offset:64
	global_load_dword v126, v[74:75], off offset:80
	global_load_dword v128, v[74:75], off offset:96
	global_load_dword v130, v[74:75], off offset:112
	global_load_dword v132, v[74:75], off offset:128
	global_load_dword v134, v[74:75], off offset:144
	global_load_dword v136, v[74:75], off offset:160
	global_load_dword v138, v[74:75], off offset:176
	global_load_dword v140, v[74:75], off offset:192
	global_load_dword v142, v[74:75], off offset:208
	global_load_dword v144, v[74:75], off offset:224
	global_load_dword v146, v[74:75], off offset:240
	v_add_co_u32_e32 v2, vcc, s81, v0
	s_mov_b32 s1, 0x54000
	s_nop 0
	v_addc_co_u32_e32 v3, vcc, 0, v1, vcc
	global_load_dwordx4 v[8:11], v[2:3], off
	v_add_co_u32_e32 v2, vcc, s82, v0
	s_lshl_b32 s0, s0, 7
	s_nop 0
	v_addc_co_u32_e32 v3, vcc, 0, v1, vcc
	global_load_dwordx4 v[12:15], v[2:3], off
	v_add_co_u32_e32 v2, vcc, s85, v0
	s_and_b32 s0, s0, 0xffffff00
	s_nop 0
	v_addc_co_u32_e32 v3, vcc, 0, v1, vcc
	global_load_dwordx4 v[16:19], v[2:3], off
	v_add_co_u32_e32 v2, vcc, s34, v0
	s_and_b32 s8, s8, 64
	s_nop 0
	v_addc_co_u32_e32 v3, vcc, 0, v1, vcc
	global_load_dwordx4 v[20:23], v[2:3], off
	v_add_co_u32_e32 v2, vcc, s88, v0
	s_or_b32 s0, s8, s0
	s_nop 0
	v_addc_co_u32_e32 v3, vcc, 0, v1, vcc
	global_load_dwordx4 v[24:27], v[2:3], off
	v_add_co_u32_e32 v2, vcc, s86, v0
	s_ashr_i32 s9, s12, 31
	s_nop 0
	v_addc_co_u32_e32 v3, vcc, 0, v1, vcc
	global_load_dwordx4 v[28:31], v[2:3], off
	v_add_co_u32_e32 v2, vcc, s1, v0
	s_mov_b32 s1, 0x6c000
	s_nop 0
	v_addc_co_u32_e32 v3, vcc, 0, v1, vcc
	global_load_dwordx4 v[32:35], v[2:3], off
	v_add_co_u32_e32 v2, vcc, s53, v0
	s_add_u32 s8, s10, s12
	s_nop 0
	v_addc_co_u32_e32 v3, vcc, 0, v1, vcc
	global_load_dwordx4 v[36:39], v[2:3], off
	v_add_co_u32_e32 v2, vcc, s1, v0
	s_mov_b32 s1, 0x84000
	s_nop 0
	v_addc_co_u32_e32 v3, vcc, 0, v1, vcc
	global_load_dwordx4 v[44:47], v[2:3], off
	v_add_co_u32_e32 v2, vcc, s89, v0
	s_addc_u32 s9, s11, s9
	s_nop 0
	v_addc_co_u32_e32 v3, vcc, 0, v1, vcc
	global_load_dwordx4 v[52:55], v[2:3], off
	v_add_co_u32_e32 v2, vcc, s1, v0
	s_mov_b32 s1, 0x9c000
	s_nop 0
	v_addc_co_u32_e32 v3, vcc, 0, v1, vcc
	global_load_dwordx4 v[60:63], v[2:3], off
	v_add_co_u32_e32 v2, vcc, s95, v0
	v_readlane_b32 s37, v254, 4
	s_nop 0
	v_addc_co_u32_e32 v3, vcc, 0, v1, vcc
	global_load_dwordx4 v[56:59], v[2:3], off
	v_add_co_u32_e32 v2, vcc, s1, v0
	s_mov_b32 s1, 0xb4000
	s_nop 0
	v_addc_co_u32_e32 v3, vcc, 0, v1, vcc
	global_load_dwordx4 v[48:51], v[2:3], off
	v_add_co_u32_e32 v2, vcc, s80, v0
	v_addc_co_u32_e32 v3, vcc, 0, v1, vcc
	v_add_co_u32_e32 v0, vcc, s1, v0
	global_load_dwordx4 v[40:43], v[2:3], off
	s_nop 0
	v_addc_co_u32_e32 v1, vcc, 0, v1, vcc
	global_load_dwordx4 v[0:3], v[0:1], off
	v_readlane_b32 s38, v254, 5
	v_readlane_b32 s39, v254, 6
	v_readlane_b32 s40, v254, 7
	v_readlane_b32 s41, v254, 8
	v_readlane_b32 s42, v254, 9
	v_readlane_b32 s43, v254, 10
	v_readlane_b32 s44, v254, 11
	v_readlane_b32 s45, v254, 12
	v_readlane_b32 s46, v254, 13
	v_readlane_b32 s47, v254, 14
	v_readlane_b32 s48, v254, 15
	v_readlane_b32 s49, v254, 16
	s_waitcnt vmcnt(0)
	v_pk_mul_f32 v[4:5], v[4:5], v[116:117] op_sel_hi:[1,0]
	v_pk_mul_f32 v[6:7], v[6:7], v[116:117] op_sel_hi:[1,0]
	v_pk_mul_f32 v[10:11], v[10:11], v[118:119] op_sel_hi:[1,0]
	v_pk_mul_f32 v[8:9], v[8:9], v[118:119] op_sel_hi:[1,0]
	v_pk_mul_f32 v[14:15], v[14:15], v[120:121] op_sel_hi:[1,0]
	v_pk_mul_f32 v[12:13], v[12:13], v[120:121] op_sel_hi:[1,0]
	v_pk_mul_f32 v[18:19], v[18:19], v[122:123] op_sel_hi:[1,0]
	v_pk_mul_f32 v[16:17], v[16:17], v[122:123] op_sel_hi:[1,0]
	v_pk_mul_f32 v[22:23], v[22:23], v[124:125] op_sel_hi:[1,0]
	v_pk_mul_f32 v[20:21], v[20:21], v[124:125] op_sel_hi:[1,0]
	v_pk_mul_f32 v[26:27], v[26:27], v[126:127] op_sel_hi:[1,0]
	v_pk_mul_f32 v[24:25], v[24:25], v[126:127] op_sel_hi:[1,0]
	v_pk_mul_f32 v[30:31], v[30:31], v[128:129] op_sel_hi:[1,0]
	v_pk_mul_f32 v[28:29], v[28:29], v[128:129] op_sel_hi:[1,0]
	v_pk_mul_f32 v[34:35], v[34:35], v[130:131] op_sel_hi:[1,0]
	v_pk_mul_f32 v[32:33], v[32:33], v[130:131] op_sel_hi:[1,0]
	v_pk_mul_f32 v[38:39], v[38:39], v[132:133] op_sel_hi:[1,0]
	v_pk_mul_f32 v[36:37], v[36:37], v[132:133] op_sel_hi:[1,0]
	v_pk_mul_f32 v[46:47], v[46:47], v[134:135] op_sel_hi:[1,0]
	v_pk_mul_f32 v[44:45], v[44:45], v[134:135] op_sel_hi:[1,0]
	v_pk_mul_f32 v[54:55], v[54:55], v[136:137] op_sel_hi:[1,0]
	v_pk_mul_f32 v[52:53], v[52:53], v[136:137] op_sel_hi:[1,0]
	v_pk_mul_f32 v[62:63], v[62:63], v[138:139] op_sel_hi:[1,0]
	v_pk_mul_f32 v[60:61], v[60:61], v[138:139] op_sel_hi:[1,0]
	v_pk_mul_f32 v[58:59], v[58:59], v[140:141] op_sel_hi:[1,0]
	v_pk_mul_f32 v[56:57], v[56:57], v[140:141] op_sel_hi:[1,0]
	v_pk_mul_f32 v[50:51], v[50:51], v[142:143] op_sel_hi:[1,0]
	v_pk_mul_f32 v[48:49], v[48:49], v[142:143] op_sel_hi:[1,0]
	v_pk_mul_f32 v[42:43], v[42:43], v[144:145] op_sel_hi:[1,0]
	v_pk_mul_f32 v[40:41], v[40:41], v[144:145] op_sel_hi:[1,0]
	v_pk_mul_f32 v[2:3], v[2:3], v[146:147] op_sel_hi:[1,0]
	v_pk_mul_f32 v[0:1], v[0:1], v[146:147] op_sel_hi:[1,0]
	ds_write_b128 v78, v[4:7]
	ds_write_b128 v78, v[8:11] offset:1088
	ds_write_b128 v78, v[12:15] offset:2176
	ds_write_b128 v78, v[16:19] offset:3264
	ds_write_b128 v79, v[20:23] offset:4352
	ds_write_b128 v79, v[24:27] offset:5440
	ds_write_b128 v79, v[28:31] offset:6528
	ds_write_b128 v79, v[32:35] offset:7616
	ds_write_b128 v80, v[36:39] offset:8704
	ds_write_b128 v80, v[44:47] offset:9792
	ds_write_b128 v80, v[52:55] offset:10880
	ds_write_b128 v80, v[60:63] offset:11968
	ds_write_b128 v81, v[56:59] offset:13056
	ds_write_b128 v81, v[48:51] offset:14144
	ds_write_b128 v81, v[40:43] offset:15232
	ds_write_b128 v81, v[0:3] offset:16320
	s_waitcnt lgkmcnt(0)
	ds_read2_b32 v[2:3], v83 offset1:68
	v_lshl_add_u64 v[0:1], s[8:9], 0, v[66:67]
	s_waitcnt lgkmcnt(0)
	v_mul_f32_e32 v4, 0x42800000, v2
	v_mul_f32_e32 v5, 0x42800000, v3
	ds_read2_b32 v[2:3], v83 offset0:136 offset1:204
	s_waitcnt lgkmcnt(0)
	v_mul_f32_e32 v6, 0x42800000, v2
	v_mov_b32_e32 v2, v65
	v_cvt_pk_fp8_f32 v2, v4, v5
	ds_read2_b32 v[4:5], v110 offset0:16 offset1:84
	v_mul_f32_e32 v3, 0x42800000, v3
	v_cvt_pk_fp8_f32 v2, v6, v3 op_sel:[0,0,1]
	v_mov_b32_e32 v3, v65
	s_waitcnt lgkmcnt(0)
	v_mul_f32_e32 v6, 0x42800000, v4
	v_mul_f32_e32 v7, 0x42800000, v5
	ds_read2_b32 v[4:5], v110 offset0:152 offset1:220
	v_cvt_pk_fp8_f32 v3, v6, v7
	v_add_u32_e32 v6, 0x800, v83
	s_waitcnt lgkmcnt(0)
	v_mul_f32_e32 v4, 0x42800000, v4
	v_mul_f32_e32 v5, 0x42800000, v5
	v_cvt_pk_fp8_f32 v3, v4, v5 op_sel:[0,0,1]
	ds_read2_b32 v[4:5], v6 offset0:32 offset1:100
	s_waitcnt lgkmcnt(0)
	v_mul_f32_e32 v7, 0x42800000, v4
	v_mul_f32_e32 v8, 0x42800000, v5
	ds_read2_b32 v[4:5], v6 offset0:168 offset1:236
	s_waitcnt lgkmcnt(0)
	v_mul_f32_e32 v6, 0x42800000, v4
	v_mov_b32_e32 v4, v65
	v_cvt_pk_fp8_f32 v4, v7, v8
	v_mul_f32_e32 v5, 0x42800000, v5
	v_cvt_pk_fp8_f32 v4, v6, v5 op_sel:[0,0,1]
	v_add_u32_e32 v5, 0xc00, v83
	ds_read2_b32 v[6:7], v5 offset0:48 offset1:116
	s_waitcnt lgkmcnt(0)
	v_mul_f32_e32 v8, 0x42800000, v6
	v_mul_f32_e32 v9, 0x42800000, v7
	ds_read2_b32 v[6:7], v5 offset0:184 offset1:252
	v_mov_b32_e32 v5, v65
	v_cvt_pk_fp8_f32 v5, v8, v9
	s_waitcnt lgkmcnt(0)
	v_mul_f32_e32 v6, 0x42800000, v6
	v_mul_f32_e32 v7, 0x42800000, v7
	v_cvt_pk_fp8_f32 v5, v6, v7 op_sel:[0,0,1]
	v_add_u32_e32 v6, s0, v82
	v_ashrrev_i32_e32 v7, 31, v6
	v_lshlrev_b64 v[6:7], 12, v[6:7]
	v_lshl_add_u64 v[6:7], v[0:1], 0, v[6:7]
	global_store_dwordx4 v[6:7], v[2:5], off
	ds_read2_b32 v[2:3], v85 offset1:68
	s_waitcnt lgkmcnt(0)
	v_mul_f32_e32 v4, 0x42800000, v2
	v_mul_f32_e32 v5, 0x42800000, v3
	ds_read2_b32 v[2:3], v85 offset0:136 offset1:204
	s_waitcnt lgkmcnt(0)
	v_mul_f32_e32 v6, 0x42800000, v2
	v_mov_b32_e32 v2, v65
	v_cvt_pk_fp8_f32 v2, v4, v5
	v_mul_f32_e32 v3, 0x42800000, v3
	v_cvt_pk_fp8_f32 v2, v6, v3 op_sel:[0,0,1]
	v_add_u32_e32 v3, 0x400, v85
	ds_read2_b32 v[4:5], v3 offset0:16 offset1:84
	s_waitcnt lgkmcnt(0)
	v_mul_f32_e32 v6, 0x42800000, v4
	v_mul_f32_e32 v7, 0x42800000, v5
	ds_read2_b32 v[4:5], v3 offset0:152 offset1:220
	v_mov_b32_e32 v3, v65
	v_cvt_pk_fp8_f32 v3, v6, v7
	v_add_u32_e32 v6, 0x800, v85
	s_waitcnt lgkmcnt(0)
	v_mul_f32_e32 v4, 0x42800000, v4
	v_mul_f32_e32 v5, 0x42800000, v5
	v_cvt_pk_fp8_f32 v3, v4, v5 op_sel:[0,0,1]
	ds_read2_b32 v[4:5], v6 offset0:32 offset1:100
	s_waitcnt lgkmcnt(0)
	v_mul_f32_e32 v7, 0x42800000, v4
	v_mul_f32_e32 v8, 0x42800000, v5
	ds_read2_b32 v[4:5], v6 offset0:168 offset1:236
	s_waitcnt lgkmcnt(0)
	v_mul_f32_e32 v6, 0x42800000, v4
	v_mov_b32_e32 v4, v65
	v_cvt_pk_fp8_f32 v4, v7, v8
	v_mul_f32_e32 v5, 0x42800000, v5
	v_cvt_pk_fp8_f32 v4, v6, v5 op_sel:[0,0,1]
	v_add_u32_e32 v5, 0xc00, v85
	ds_read2_b32 v[6:7], v5 offset0:48 offset1:116
	s_waitcnt lgkmcnt(0)
	v_mul_f32_e32 v8, 0x42800000, v6
	v_mul_f32_e32 v9, 0x42800000, v7
	ds_read2_b32 v[6:7], v5 offset0:184 offset1:252
	v_mov_b32_e32 v5, v65
	v_cvt_pk_fp8_f32 v5, v8, v9
	s_waitcnt lgkmcnt(0)
	v_mul_f32_e32 v6, 0x42800000, v6
	v_mul_f32_e32 v7, 0x42800000, v7
	v_cvt_pk_fp8_f32 v5, v6, v7 op_sel:[0,0,1]
	v_add_u32_e32 v6, s0, v84
	v_ashrrev_i32_e32 v7, 31, v6
	v_lshlrev_b64 v[6:7], 12, v[6:7]
	v_lshl_add_u64 v[6:7], v[0:1], 0, v[6:7]
	global_store_dwordx4 v[6:7], v[2:5], off
	ds_read2_b32 v[2:3], v87 offset1:68
	s_waitcnt lgkmcnt(0)
	v_mul_f32_e32 v4, 0x42800000, v2
	v_mul_f32_e32 v5, 0x42800000, v3
	ds_read2_b32 v[2:3], v87 offset0:136 offset1:204
	s_waitcnt lgkmcnt(0)
	v_mul_f32_e32 v6, 0x42800000, v2
	v_mov_b32_e32 v2, v65
	v_cvt_pk_fp8_f32 v2, v4, v5
	v_mul_f32_e32 v3, 0x42800000, v3
	v_cvt_pk_fp8_f32 v2, v6, v3 op_sel:[0,0,1]
	v_add_u32_e32 v3, 0x400, v87
	ds_read2_b32 v[4:5], v3 offset0:16 offset1:84
	s_waitcnt lgkmcnt(0)
	v_mul_f32_e32 v6, 0x42800000, v4
	v_mul_f32_e32 v7, 0x42800000, v5
	ds_read2_b32 v[4:5], v3 offset0:152 offset1:220
	v_mov_b32_e32 v3, v65
	v_cvt_pk_fp8_f32 v3, v6, v7
	v_add_u32_e32 v6, 0x800, v87
	s_waitcnt lgkmcnt(0)
	v_mul_f32_e32 v4, 0x42800000, v4
	v_mul_f32_e32 v5, 0x42800000, v5
	v_cvt_pk_fp8_f32 v3, v4, v5 op_sel:[0,0,1]
	ds_read2_b32 v[4:5], v6 offset0:32 offset1:100
	s_waitcnt lgkmcnt(0)
	v_mul_f32_e32 v7, 0x42800000, v4
	v_mul_f32_e32 v8, 0x42800000, v5
	ds_read2_b32 v[4:5], v6 offset0:168 offset1:236
	s_waitcnt lgkmcnt(0)
	v_mul_f32_e32 v6, 0x42800000, v4
	v_mov_b32_e32 v4, v65
	v_cvt_pk_fp8_f32 v4, v7, v8
	v_mul_f32_e32 v5, 0x42800000, v5
	v_cvt_pk_fp8_f32 v4, v6, v5 op_sel:[0,0,1]
	v_add_u32_e32 v5, 0xc00, v87
	ds_read2_b32 v[6:7], v5 offset0:48 offset1:116
	s_waitcnt lgkmcnt(0)
	v_mul_f32_e32 v8, 0x42800000, v6
	v_mul_f32_e32 v9, 0x42800000, v7
	ds_read2_b32 v[6:7], v5 offset0:184 offset1:252
	v_mov_b32_e32 v5, v65
	v_cvt_pk_fp8_f32 v5, v8, v9
	s_waitcnt lgkmcnt(0)
	v_mul_f32_e32 v6, 0x42800000, v6
	v_mul_f32_e32 v7, 0x42800000, v7
	v_cvt_pk_fp8_f32 v5, v6, v7 op_sel:[0,0,1]
	v_add_u32_e32 v6, s0, v86
	v_ashrrev_i32_e32 v7, 31, v6
	v_lshlrev_b64 v[6:7], 12, v[6:7]
	v_lshl_add_u64 v[6:7], v[0:1], 0, v[6:7]
	global_store_dwordx4 v[6:7], v[2:5], off
	ds_read2_b32 v[2:3], v89 offset1:68
	s_waitcnt lgkmcnt(0)
	v_mul_f32_e32 v4, 0x42800000, v2
	v_mul_f32_e32 v5, 0x42800000, v3
	ds_read2_b32 v[2:3], v89 offset0:136 offset1:204
	s_waitcnt lgkmcnt(0)
	v_mul_f32_e32 v6, 0x42800000, v2
	v_mov_b32_e32 v2, v65
	v_cvt_pk_fp8_f32 v2, v4, v5
	v_mul_f32_e32 v3, 0x42800000, v3
	v_cvt_pk_fp8_f32 v2, v6, v3 op_sel:[0,0,1]
	v_add_u32_e32 v3, 0x400, v89
	ds_read2_b32 v[4:5], v3 offset0:16 offset1:84
	s_waitcnt lgkmcnt(0)
	v_mul_f32_e32 v6, 0x42800000, v4
	v_mul_f32_e32 v7, 0x42800000, v5
	ds_read2_b32 v[4:5], v3 offset0:152 offset1:220
	v_mov_b32_e32 v3, v65
	v_cvt_pk_fp8_f32 v3, v6, v7
	v_add_u32_e32 v6, 0x800, v89
	s_waitcnt lgkmcnt(0)
	v_mul_f32_e32 v4, 0x42800000, v4
	v_mul_f32_e32 v5, 0x42800000, v5
	v_cvt_pk_fp8_f32 v3, v4, v5 op_sel:[0,0,1]
	ds_read2_b32 v[4:5], v6 offset0:32 offset1:100
	s_waitcnt lgkmcnt(0)
	v_mul_f32_e32 v7, 0x42800000, v4
	v_mul_f32_e32 v8, 0x42800000, v5
	ds_read2_b32 v[4:5], v6 offset0:168 offset1:236
	s_waitcnt lgkmcnt(0)
	v_mul_f32_e32 v6, 0x42800000, v4
	v_mov_b32_e32 v4, v65
	v_cvt_pk_fp8_f32 v4, v7, v8
	v_mul_f32_e32 v5, 0x42800000, v5
	v_cvt_pk_fp8_f32 v4, v6, v5 op_sel:[0,0,1]
	v_add_u32_e32 v5, 0xc00, v89
	ds_read2_b32 v[6:7], v5 offset0:48 offset1:116
	s_waitcnt lgkmcnt(0)
	v_mul_f32_e32 v8, 0x42800000, v6
	v_mul_f32_e32 v9, 0x42800000, v7
	ds_read2_b32 v[6:7], v5 offset0:184 offset1:252
	v_mov_b32_e32 v5, v65
	v_cvt_pk_fp8_f32 v5, v8, v9
	s_waitcnt lgkmcnt(0)
	v_mul_f32_e32 v6, 0x42800000, v6
	v_mul_f32_e32 v7, 0x42800000, v7
	v_cvt_pk_fp8_f32 v5, v6, v7 op_sel:[0,0,1]
	v_add_u32_e32 v6, s0, v88
	v_ashrrev_i32_e32 v7, 31, v6
	v_lshlrev_b64 v[6:7], 12, v[6:7]
	v_lshl_add_u64 v[0:1], v[0:1], 0, v[6:7]
	global_store_dwordx4 v[0:1], v[2:5], off
	s_waitcnt lgkmcnt(0)

.LBB0_89:
	s_andn2_b64 vcc, exec, s[8:9]
	s_cbranch_vccnz .LBB0_93
	s_add_i32 s0, s66, 0xffffb600
	s_mul_i32 s8, s0, 0xaaab
	s_lshr_b32 s8, s8, 22
	s_mul_i32 s10, s8, 0xffffffa0
	v_readlane_b32 s36, v254, 3
	s_add_i32 s10, s10, s0
	s_lshl_b32 s96, s8, 6
	v_readlane_b32 s44, v254, 11
	v_readlane_b32 s45, v254, 12
	s_lshl_b32 s8, s10, 6
	v_add_u32_e32 v74, s96, v77
	v_mov_b64_e32 v[0:1], s[44:45]
	s_movk_i32 s0, 0x6000
	v_mad_i64_i32 v[0:1], s[12:13], v74, s0, v[0:1]
	s_ashr_i32 s9, s8, 31
	v_lshl_add_u64 v[0:1], s[8:9], 2, v[0:1]
	v_lshl_add_u64 v[56:57], v[0:1], 0, v[64:65]
	v_add_co_u32_e32 v4, vcc, s82, v56
	s_mov_b32 s0, 0xd8000
	s_nop 0
	v_addc_co_u32_e32 v5, vcc, 0, v57, vcc
	v_add_co_u32_e32 v8, vcc, s34, v56
	global_load_dwordx4 v[0:3], v[56:57], off
	s_nop 0
	global_load_dwordx4 v[4:7], v[4:5], off
	v_addc_co_u32_e32 v9, vcc, 0, v57, vcc
	v_add_co_u32_e32 v12, vcc, s86, v56
	v_readlane_b32 s37, v254, 4
	s_nop 0
	v_addc_co_u32_e32 v13, vcc, 0, v57, vcc
	v_add_co_u32_e32 v16, vcc, s53, v56
	global_load_dwordx4 v[8:11], v[8:9], off
	s_nop 0
	global_load_dwordx4 v[12:15], v[12:13], off
	v_addc_co_u32_e32 v17, vcc, 0, v57, vcc
	v_add_co_u32_e32 v20, vcc, s89, v56
	v_readlane_b32 s38, v254, 5
	s_nop 0
	v_addc_co_u32_e32 v21, vcc, 0, v57, vcc
	v_add_co_u32_e32 v24, vcc, s95, v56
	global_load_dwordx4 v[16:19], v[16:17], off
	s_nop 0
	global_load_dwordx4 v[20:23], v[20:21], off
	v_addc_co_u32_e32 v25, vcc, 0, v57, vcc
	v_add_co_u32_e32 v28, vcc, s80, v56
	v_readlane_b32 s39, v254, 6
	s_nop 0
	v_addc_co_u32_e32 v29, vcc, 0, v57, vcc
	v_add_co_u32_e32 v32, vcc, s59, v56
	global_load_dwordx4 v[24:27], v[24:25], off
	s_nop 0
	global_load_dwordx4 v[28:31], v[28:29], off
	v_addc_co_u32_e32 v33, vcc, 0, v57, vcc
	v_add_co_u32_e32 v36, vcc, s0, v56
	v_readlane_b32 s40, v254, 7
	s_nop 0
	v_addc_co_u32_e32 v37, vcc, 0, v57, vcc
	v_add_co_u32_e32 v40, vcc, s58, v56
	global_load_dwordx4 v[32:35], v[32:33], off
	s_nop 0
	global_load_dwordx4 v[36:39], v[36:37], off
	v_addc_co_u32_e32 v41, vcc, 0, v57, vcc
	v_add_co_u32_e32 v44, vcc, s64, v56
	v_readlane_b32 s41, v254, 8
	s_nop 0
	v_addc_co_u32_e32 v45, vcc, 0, v57, vcc
	v_add_co_u32_e32 v48, vcc, s65, v56
	global_load_dwordx4 v[40:43], v[40:41], off
	s_nop 0
	global_load_dwordx4 v[44:47], v[44:45], off
	v_addc_co_u32_e32 v49, vcc, 0, v57, vcc
	v_add_co_u32_e32 v52, vcc, 0x138000, v56
	v_readlane_b32 s42, v254, 9
	s_nop 0
	v_addc_co_u32_e32 v53, vcc, 0, v57, vcc
	v_add_co_u32_e32 v58, vcc, 0x150000, v56
	global_load_dwordx4 v[48:51], v[48:49], off
	s_nop 0
	global_load_dwordx4 v[52:55], v[52:53], off
	v_addc_co_u32_e32 v59, vcc, 0, v57, vcc
	v_add_co_u32_e32 v60, vcc, 0x168000, v56
	v_readlane_b32 s43, v254, 10
	s_nop 0
	v_addc_co_u32_e32 v61, vcc, 0, v57, vcc
	global_load_dwordx4 v[56:59], v[58:59], off
	s_nop 0
	global_load_dwordx4 v[60:63], v[60:61], off
	s_andn2_b64 vcc, exec, s[56:57]
	v_readlane_b32 s46, v254, 13
	v_readlane_b32 s47, v254, 14
	v_readlane_b32 s48, v254, 15
	v_readlane_b32 s49, v254, 16
	v_readlane_b32 s50, v254, 17
	v_readlane_b32 s51, v254, 18
	s_cbranch_vccnz .LBB0_92
	v_readlane_b32 s36, v253, 17
	v_ashrrev_i32_e32 v75, 31, v74
	v_readlane_b32 s42, v253, 23
	v_readlane_b32 s43, v253, 24
	v_readlane_b32 s37, v253, 18
	v_readlane_b32 s38, v253, 19
	v_lshl_add_u64 v[74:75], v[74:75], 2, s[42:43]
	global_load_dword v116, v[74:75], off
	global_load_dword v118, v[74:75], off offset:16
	global_load_dword v120, v[74:75], off offset:32
	global_load_dword v122, v[74:75], off offset:48
	global_load_dword v124, v[74:75], off offset:64
	global_load_dword v126, v[74:75], off offset:80
	global_load_dword v128, v[74:75], off offset:96
	global_load_dword v130, v[74:75], off offset:112
	global_load_dword v132, v[74:75], off offset:128
	global_load_dword v134, v[74:75], off offset:144
	global_load_dword v136, v[74:75], off offset:160
	global_load_dword v138, v[74:75], off offset:176
	global_load_dword v140, v[74:75], off offset:192
	global_load_dword v142, v[74:75], off offset:208
	global_load_dword v144, v[74:75], off offset:224
	global_load_dword v146, v[74:75], off offset:240
	v_readlane_b32 s39, v253, 20
	v_readlane_b32 s40, v253, 21
	v_readlane_b32 s41, v253, 22
	v_readlane_b32 s44, v253, 25
	v_readlane_b32 s45, v253, 26
	v_readlane_b32 s46, v253, 27
	v_readlane_b32 s47, v253, 28
	v_readlane_b32 s48, v253, 29
	v_readlane_b32 s49, v253, 30
	v_readlane_b32 s50, v253, 31
	v_readlane_b32 s51, v253, 32
	s_waitcnt vmcnt(0)
	v_pk_mul_f32 v[2:3], v[2:3], v[116:117] op_sel_hi:[1,0]
	v_pk_mul_f32 v[0:1], v[0:1], v[116:117] op_sel_hi:[1,0]
	v_pk_mul_f32 v[6:7], v[6:7], v[118:119] op_sel_hi:[1,0]
	v_pk_mul_f32 v[4:5], v[4:5], v[118:119] op_sel_hi:[1,0]
	v_pk_mul_f32 v[10:11], v[10:11], v[120:121] op_sel_hi:[1,0]
	v_pk_mul_f32 v[8:9], v[8:9], v[120:121] op_sel_hi:[1,0]
	v_pk_mul_f32 v[14:15], v[14:15], v[122:123] op_sel_hi:[1,0]
	v_pk_mul_f32 v[12:13], v[12:13], v[122:123] op_sel_hi:[1,0]
	v_pk_mul_f32 v[18:19], v[18:19], v[124:125] op_sel_hi:[1,0]
	v_pk_mul_f32 v[16:17], v[16:17], v[124:125] op_sel_hi:[1,0]
	v_pk_mul_f32 v[22:23], v[22:23], v[126:127] op_sel_hi:[1,0]
	v_pk_mul_f32 v[20:21], v[20:21], v[126:127] op_sel_hi:[1,0]
	v_pk_mul_f32 v[26:27], v[26:27], v[128:129] op_sel_hi:[1,0]
	v_pk_mul_f32 v[24:25], v[24:25], v[128:129] op_sel_hi:[1,0]
	v_pk_mul_f32 v[30:31], v[30:31], v[130:131] op_sel_hi:[1,0]
	v_pk_mul_f32 v[28:29], v[28:29], v[130:131] op_sel_hi:[1,0]
	v_pk_mul_f32 v[34:35], v[34:35], v[132:133] op_sel_hi:[1,0]
	v_pk_mul_f32 v[32:33], v[32:33], v[132:133] op_sel_hi:[1,0]
	v_pk_mul_f32 v[38:39], v[38:39], v[134:135] op_sel_hi:[1,0]
	v_pk_mul_f32 v[36:37], v[36:37], v[134:135] op_sel_hi:[1,0]
	v_pk_mul_f32 v[42:43], v[42:43], v[136:137] op_sel_hi:[1,0]
	v_pk_mul_f32 v[40:41], v[40:41], v[136:137] op_sel_hi:[1,0]
	v_pk_mul_f32 v[46:47], v[46:47], v[138:139] op_sel_hi:[1,0]
	v_pk_mul_f32 v[44:45], v[44:45], v[138:139] op_sel_hi:[1,0]
	v_pk_mul_f32 v[50:51], v[50:51], v[140:141] op_sel_hi:[1,0]
	v_pk_mul_f32 v[48:49], v[48:49], v[140:141] op_sel_hi:[1,0]
	v_pk_mul_f32 v[54:55], v[54:55], v[142:143] op_sel_hi:[1,0]
	v_pk_mul_f32 v[52:53], v[52:53], v[142:143] op_sel_hi:[1,0]
	v_pk_mul_f32 v[58:59], v[58:59], v[144:145] op_sel_hi:[1,0]
	v_pk_mul_f32 v[56:57], v[56:57], v[144:145] op_sel_hi:[1,0]
	v_pk_mul_f32 v[62:63], v[62:63], v[146:147] op_sel_hi:[1,0]
	v_pk_mul_f32 v[60:61], v[60:61], v[146:147] op_sel_hi:[1,0]

.LBB0_94:
	s_andn2_b64 vcc, exec, s[8:9]
	s_cbranch_vccnz .LBB0_98
	s_add_i32 s0, s66, 0xffffce00
	s_mul_i32 s8, s0, 0xaaab
	s_lshr_b32 s8, s8, 22
	s_mul_i32 s10, s8, 0xffffffa0
	v_readlane_b32 s36, v254, 3
	s_add_i32 s10, s10, s0
	s_lshl_b32 s96, s8, 6
	v_readlane_b32 s42, v254, 9
	v_readlane_b32 s43, v254, 10
	s_lshl_b32 s8, s10, 6
	v_add_u32_e32 v74, s96, v77
	v_mov_b64_e32 v[0:1], s[42:43]
	s_movk_i32 s0, 0x6000
	v_mad_i64_i32 v[0:1], s[12:13], v74, s0, v[0:1]
	s_ashr_i32 s9, s8, 31
	v_lshl_add_u64 v[0:1], s[8:9], 2, v[0:1]
	v_lshl_add_u64 v[56:57], v[0:1], 0, v[64:65]
	v_add_co_u32_e32 v4, vcc, s82, v56
	s_mov_b32 s0, 0xd8000
	s_nop 0
	v_addc_co_u32_e32 v5, vcc, 0, v57, vcc
	v_add_co_u32_e32 v8, vcc, s34, v56
	global_load_dwordx4 v[0:3], v[56:57], off
	s_nop 0
	global_load_dwordx4 v[4:7], v[4:5], off
	v_addc_co_u32_e32 v9, vcc, 0, v57, vcc
	v_add_co_u32_e32 v12, vcc, s86, v56
	v_readlane_b32 s37, v254, 4
	s_nop 0
	v_addc_co_u32_e32 v13, vcc, 0, v57, vcc
	v_add_co_u32_e32 v16, vcc, s53, v56
	global_load_dwordx4 v[8:11], v[8:9], off
	s_nop 0
	global_load_dwordx4 v[12:15], v[12:13], off
	v_addc_co_u32_e32 v17, vcc, 0, v57, vcc
	v_add_co_u32_e32 v20, vcc, s89, v56
	v_readlane_b32 s38, v254, 5
	s_nop 0
	v_addc_co_u32_e32 v21, vcc, 0, v57, vcc
	v_add_co_u32_e32 v24, vcc, s95, v56
	global_load_dwordx4 v[16:19], v[16:17], off
	s_nop 0
	global_load_dwordx4 v[20:23], v[20:21], off
	v_addc_co_u32_e32 v25, vcc, 0, v57, vcc
	v_add_co_u32_e32 v28, vcc, s80, v56
	v_readlane_b32 s39, v254, 6
	s_nop 0
	v_addc_co_u32_e32 v29, vcc, 0, v57, vcc
	v_add_co_u32_e32 v32, vcc, s59, v56
	global_load_dwordx4 v[24:27], v[24:25], off
	s_nop 0
	global_load_dwordx4 v[28:31], v[28:29], off
	v_addc_co_u32_e32 v33, vcc, 0, v57, vcc
	v_add_co_u32_e32 v36, vcc, s0, v56
	v_readlane_b32 s40, v254, 7
	s_nop 0
	v_addc_co_u32_e32 v37, vcc, 0, v57, vcc
	v_add_co_u32_e32 v40, vcc, s58, v56
	global_load_dwordx4 v[32:35], v[32:33], off
	s_nop 0
	global_load_dwordx4 v[36:39], v[36:37], off
	v_addc_co_u32_e32 v41, vcc, 0, v57, vcc
	v_add_co_u32_e32 v44, vcc, s64, v56
	v_readlane_b32 s41, v254, 8
	s_nop 0
	v_addc_co_u32_e32 v45, vcc, 0, v57, vcc
	v_add_co_u32_e32 v48, vcc, s65, v56
	global_load_dwordx4 v[40:43], v[40:41], off
	s_nop 0
	global_load_dwordx4 v[44:47], v[44:45], off
	v_addc_co_u32_e32 v49, vcc, 0, v57, vcc
	v_add_co_u32_e32 v52, vcc, 0x138000, v56
	v_readlane_b32 s44, v254, 11
	s_nop 0
	v_addc_co_u32_e32 v53, vcc, 0, v57, vcc
	v_add_co_u32_e32 v58, vcc, 0x150000, v56
	global_load_dwordx4 v[48:51], v[48:49], off
	s_nop 0
	global_load_dwordx4 v[52:55], v[52:53], off
	v_addc_co_u32_e32 v59, vcc, 0, v57, vcc
	v_add_co_u32_e32 v60, vcc, 0x168000, v56
	v_readlane_b32 s45, v254, 12
	s_nop 0
	v_addc_co_u32_e32 v61, vcc, 0, v57, vcc
	global_load_dwordx4 v[56:59], v[58:59], off
	s_nop 0
	global_load_dwordx4 v[60:63], v[60:61], off
	s_andn2_b64 vcc, exec, s[56:57]
	v_readlane_b32 s46, v254, 13
	v_readlane_b32 s47, v254, 14
	v_readlane_b32 s48, v254, 15
	v_readlane_b32 s49, v254, 16
	v_readlane_b32 s50, v254, 17
	v_readlane_b32 s51, v254, 18
	s_cbranch_vccnz .LBB0_97
	v_readlane_b32 s36, v253, 17
	v_ashrrev_i32_e32 v75, 31, v74
	v_readlane_b32 s42, v253, 23
	v_readlane_b32 s43, v253, 24
	v_readlane_b32 s37, v253, 18
	v_readlane_b32 s38, v253, 19
	v_lshl_add_u64 v[74:75], v[74:75], 2, s[42:43]
	global_load_dword v116, v[74:75], off
	global_load_dword v118, v[74:75], off offset:16
	global_load_dword v120, v[74:75], off offset:32
	global_load_dword v122, v[74:75], off offset:48
	global_load_dword v124, v[74:75], off offset:64
	global_load_dword v126, v[74:75], off offset:80
	global_load_dword v128, v[74:75], off offset:96
	global_load_dword v130, v[74:75], off offset:112
	global_load_dword v132, v[74:75], off offset:128
	global_load_dword v134, v[74:75], off offset:144
	global_load_dword v136, v[74:75], off offset:160
	global_load_dword v138, v[74:75], off offset:176
	global_load_dword v140, v[74:75], off offset:192
	global_load_dword v142, v[74:75], off offset:208
	global_load_dword v144, v[74:75], off offset:224
	global_load_dword v146, v[74:75], off offset:240
	v_readlane_b32 s39, v253, 20
	v_readlane_b32 s40, v253, 21
	v_readlane_b32 s41, v253, 22
	v_readlane_b32 s44, v253, 25
	v_readlane_b32 s45, v253, 26
	v_readlane_b32 s46, v253, 27
	v_readlane_b32 s47, v253, 28
	v_readlane_b32 s48, v253, 29
	v_readlane_b32 s49, v253, 30
	v_readlane_b32 s50, v253, 31
	v_readlane_b32 s51, v253, 32
	s_waitcnt vmcnt(0)
	v_pk_mul_f32 v[2:3], v[2:3], v[116:117] op_sel_hi:[1,0]
	v_pk_mul_f32 v[0:1], v[0:1], v[116:117] op_sel_hi:[1,0]
	v_pk_mul_f32 v[6:7], v[6:7], v[118:119] op_sel_hi:[1,0]
	v_pk_mul_f32 v[4:5], v[4:5], v[118:119] op_sel_hi:[1,0]
	v_pk_mul_f32 v[10:11], v[10:11], v[120:121] op_sel_hi:[1,0]
	v_pk_mul_f32 v[8:9], v[8:9], v[120:121] op_sel_hi:[1,0]
	v_pk_mul_f32 v[14:15], v[14:15], v[122:123] op_sel_hi:[1,0]
	v_pk_mul_f32 v[12:13], v[12:13], v[122:123] op_sel_hi:[1,0]
	v_pk_mul_f32 v[18:19], v[18:19], v[124:125] op_sel_hi:[1,0]
	v_pk_mul_f32 v[16:17], v[16:17], v[124:125] op_sel_hi:[1,0]
	v_pk_mul_f32 v[22:23], v[22:23], v[126:127] op_sel_hi:[1,0]
	v_pk_mul_f32 v[20:21], v[20:21], v[126:127] op_sel_hi:[1,0]
	v_pk_mul_f32 v[26:27], v[26:27], v[128:129] op_sel_hi:[1,0]
	v_pk_mul_f32 v[24:25], v[24:25], v[128:129] op_sel_hi:[1,0]
	v_pk_mul_f32 v[30:31], v[30:31], v[130:131] op_sel_hi:[1,0]
	v_pk_mul_f32 v[28:29], v[28:29], v[130:131] op_sel_hi:[1,0]
	v_pk_mul_f32 v[34:35], v[34:35], v[132:133] op_sel_hi:[1,0]
	v_pk_mul_f32 v[32:33], v[32:33], v[132:133] op_sel_hi:[1,0]
	v_pk_mul_f32 v[38:39], v[38:39], v[134:135] op_sel_hi:[1,0]
	v_pk_mul_f32 v[36:37], v[36:37], v[134:135] op_sel_hi:[1,0]
	v_pk_mul_f32 v[42:43], v[42:43], v[136:137] op_sel_hi:[1,0]
	v_pk_mul_f32 v[40:41], v[40:41], v[136:137] op_sel_hi:[1,0]
	v_pk_mul_f32 v[46:47], v[46:47], v[138:139] op_sel_hi:[1,0]
	v_pk_mul_f32 v[44:45], v[44:45], v[138:139] op_sel_hi:[1,0]
	v_pk_mul_f32 v[50:51], v[50:51], v[140:141] op_sel_hi:[1,0]
	v_pk_mul_f32 v[48:49], v[48:49], v[140:141] op_sel_hi:[1,0]
	v_pk_mul_f32 v[54:55], v[54:55], v[142:143] op_sel_hi:[1,0]
	v_pk_mul_f32 v[52:53], v[52:53], v[142:143] op_sel_hi:[1,0]
	v_pk_mul_f32 v[58:59], v[58:59], v[144:145] op_sel_hi:[1,0]
	v_pk_mul_f32 v[56:57], v[56:57], v[144:145] op_sel_hi:[1,0]
	v_pk_mul_f32 v[62:63], v[62:63], v[146:147] op_sel_hi:[1,0]
	v_pk_mul_f32 v[60:61], v[60:61], v[146:147] op_sel_hi:[1,0]

.LBB0_99:
	s_andn2_b64 vcc, exec, s[8:9]
	s_cbranch_vccnz .LBB0_103
	s_add_i32 s14, s66, 0xffffde00
	s_lshr_b32 s10, s14, 11
	s_lshl_b32 s96, s10, 10
	s_and_b32 s11, s14, 0x400
	s_lshl_b64 s[8:9], s[96:97], 2
	v_readlane_b32 s36, v254, 3
	v_readlane_b32 s37, v254, 4
	s_add_u32 s0, s36, s8
	v_readlane_b32 s38, v254, 5
	s_addc_u32 s12, s37, s9
	v_readlane_b32 s39, v254, 6
	s_add_u32 s8, s38, s8
	s_addc_u32 s9, s39, s9
	s_add_u32 s8, s8, 0xfffff000
	s_addc_u32 s9, s9, -1
	s_cmp_eq_u32 s11, 0
	s_mov_b32 s96, s10
	v_readlane_b32 s40, v254, 7
	s_cselect_b32 s9, s12, s9
	s_cselect_b32 s8, s0, s8
	s_lshl_b64 s[10:11], s[96:97], 25
	v_readlane_b32 s41, v254, 8
	s_add_u32 s12, s40, s10
	s_addc_u32 s13, s41, s11
	s_and_b32 s11, s14, 0x7c0
	v_add_u32_e32 v74, s11, v77
	s_lshl_b32 s10, s66, 6
	v_ashrrev_i32_e32 v75, 31, v74
	s_and_b32 s10, s10, 0xfc0
	v_lshlrev_b64 v[0:1], 14, v[74:75]
	v_lshl_add_u64 v[0:1], s[12:13], 0, v[0:1]
	s_lshl_b32 s12, s10, 2
	s_mov_b32 s13, s97
	v_lshl_add_u64 v[0:1], v[0:1], 0, s[12:13]
	v_lshl_add_u64 v[56:57], v[0:1], 0, v[64:65]
	v_add_co_u32_e32 v4, vcc, s31, v56
	s_cmp_eq_u64 s[8:9], 0
	s_nop 0
	v_addc_co_u32_e32 v5, vcc, 0, v57, vcc
	v_add_co_u32_e32 v8, vcc, s33, v56
	global_load_dwordx4 v[0:3], v[56:57], off
	s_nop 0
	global_load_dwordx4 v[4:7], v[4:5], off
	v_addc_co_u32_e32 v9, vcc, 0, v57, vcc
	v_add_co_u32_e32 v12, vcc, s34, v56
	v_readlane_b32 s42, v254, 9
	s_nop 0
	v_addc_co_u32_e32 v13, vcc, 0, v57, vcc
	v_add_co_u32_e32 v16, vcc, s35, v56
	global_load_dwordx4 v[8:11], v[8:9], off
	s_nop 0
	global_load_dwordx4 v[12:15], v[12:13], off
	v_addc_co_u32_e32 v17, vcc, 0, v57, vcc
	v_add_co_u32_e32 v20, vcc, s52, v56
	v_readlane_b32 s43, v254, 10
	s_nop 0
	v_addc_co_u32_e32 v21, vcc, 0, v57, vcc
	v_add_co_u32_e32 v24, vcc, s53, v56
	global_load_dwordx4 v[16:19], v[16:17], off
	s_nop 0
	global_load_dwordx4 v[20:23], v[20:21], off
	v_addc_co_u32_e32 v25, vcc, 0, v57, vcc
	v_add_co_u32_e32 v28, vcc, s54, v56
	v_readlane_b32 s44, v254, 11
	s_nop 0
	v_addc_co_u32_e32 v29, vcc, 0, v57, vcc
	v_add_co_u32_e32 v32, vcc, s55, v56
	global_load_dwordx4 v[24:27], v[24:25], off
	s_nop 0
	global_load_dwordx4 v[28:31], v[28:29], off
	v_addc_co_u32_e32 v33, vcc, 0, v57, vcc
	v_add_co_u32_e32 v36, vcc, s95, v56
	v_readlane_b32 s45, v254, 12
	s_nop 0
	v_addc_co_u32_e32 v37, vcc, 0, v57, vcc
	v_add_co_u32_e32 v40, vcc, s60, v56
	global_load_dwordx4 v[32:35], v[32:33], off
	s_nop 0
	global_load_dwordx4 v[36:39], v[36:37], off
	v_addc_co_u32_e32 v41, vcc, 0, v57, vcc
	v_add_co_u32_e32 v44, vcc, s30, v56
	v_readlane_b32 s46, v254, 13
	s_nop 0
	v_addc_co_u32_e32 v45, vcc, 0, v57, vcc
	v_add_co_u32_e32 v48, vcc, s59, v56
	global_load_dwordx4 v[40:43], v[40:41], off
	s_nop 0
	global_load_dwordx4 v[44:47], v[44:45], off
	v_addc_co_u32_e32 v49, vcc, 0, v57, vcc
	v_add_co_u32_e32 v52, vcc, 0xd0000, v56
	v_readlane_b32 s47, v254, 14
	s_nop 0
	v_addc_co_u32_e32 v53, vcc, 0, v57, vcc
	v_add_co_u32_e32 v58, vcc, 0xe0000, v56
	global_load_dwordx4 v[48:51], v[48:49], off
	s_nop 0
	global_load_dwordx4 v[52:55], v[52:53], off
	v_addc_co_u32_e32 v59, vcc, 0, v57, vcc
	v_add_co_u32_e32 v60, vcc, 0xf0000, v56
	v_readlane_b32 s48, v254, 15
	s_nop 0
	v_addc_co_u32_e32 v61, vcc, 0, v57, vcc
	global_load_dwordx4 v[56:59], v[58:59], off
	s_nop 0
	global_load_dwordx4 v[60:63], v[60:61], off
	v_readlane_b32 s49, v254, 16
	v_readlane_b32 s50, v254, 17
	v_readlane_b32 s51, v254, 18
	s_cbranch_scc1 .LBB0_102
	v_lshl_add_u64 v[74:75], v[74:75], 2, s[8:9]
	global_load_dword v116, v[74:75], off
	global_load_dword v118, v[74:75], off offset:16
	global_load_dword v120, v[74:75], off offset:32
	global_load_dword v122, v[74:75], off offset:48
	global_load_dword v124, v[74:75], off offset:64
	global_load_dword v126, v[74:75], off offset:80
	global_load_dword v128, v[74:75], off offset:96
	global_load_dword v130, v[74:75], off offset:112
	global_load_dword v132, v[74:75], off offset:128
	global_load_dword v134, v[74:75], off offset:144
	global_load_dword v136, v[74:75], off offset:160
	global_load_dword v138, v[74:75], off offset:176
	global_load_dword v140, v[74:75], off offset:192
	global_load_dword v142, v[74:75], off offset:208
	global_load_dword v144, v[74:75], off offset:224
	global_load_dword v146, v[74:75], off offset:240
	s_waitcnt vmcnt(0)
	v_pk_mul_f32 v[2:3], v[2:3], v[116:117] op_sel_hi:[1,0]
	v_pk_mul_f32 v[0:1], v[0:1], v[116:117] op_sel_hi:[1,0]
	v_pk_mul_f32 v[6:7], v[6:7], v[118:119] op_sel_hi:[1,0]
	v_pk_mul_f32 v[4:5], v[4:5], v[118:119] op_sel_hi:[1,0]
	v_pk_mul_f32 v[10:11], v[10:11], v[120:121] op_sel_hi:[1,0]
	v_pk_mul_f32 v[8:9], v[8:9], v[120:121] op_sel_hi:[1,0]
	v_pk_mul_f32 v[14:15], v[14:15], v[122:123] op_sel_hi:[1,0]
	v_pk_mul_f32 v[12:13], v[12:13], v[122:123] op_sel_hi:[1,0]
	v_pk_mul_f32 v[18:19], v[18:19], v[124:125] op_sel_hi:[1,0]
	v_pk_mul_f32 v[16:17], v[16:17], v[124:125] op_sel_hi:[1,0]
	v_pk_mul_f32 v[22:23], v[22:23], v[126:127] op_sel_hi:[1,0]
	v_pk_mul_f32 v[20:21], v[20:21], v[126:127] op_sel_hi:[1,0]
	v_pk_mul_f32 v[26:27], v[26:27], v[128:129] op_sel_hi:[1,0]
	v_pk_mul_f32 v[24:25], v[24:25], v[128:129] op_sel_hi:[1,0]
	v_pk_mul_f32 v[30:31], v[30:31], v[130:131] op_sel_hi:[1,0]
	v_pk_mul_f32 v[28:29], v[28:29], v[130:131] op_sel_hi:[1,0]
	v_pk_mul_f32 v[34:35], v[34:35], v[132:133] op_sel_hi:[1,0]
	v_pk_mul_f32 v[32:33], v[32:33], v[132:133] op_sel_hi:[1,0]
	v_pk_mul_f32 v[38:39], v[38:39], v[134:135] op_sel_hi:[1,0]
	v_pk_mul_f32 v[36:37], v[36:37], v[134:135] op_sel_hi:[1,0]
	v_pk_mul_f32 v[42:43], v[42:43], v[136:137] op_sel_hi:[1,0]
	v_pk_mul_f32 v[40:41], v[40:41], v[136:137] op_sel_hi:[1,0]
	v_pk_mul_f32 v[46:47], v[46:47], v[138:139] op_sel_hi:[1,0]
	v_pk_mul_f32 v[44:45], v[44:45], v[138:139] op_sel_hi:[1,0]
	v_pk_mul_f32 v[50:51], v[50:51], v[140:141] op_sel_hi:[1,0]
	v_pk_mul_f32 v[48:49], v[48:49], v[140:141] op_sel_hi:[1,0]
	v_pk_mul_f32 v[54:55], v[54:55], v[142:143] op_sel_hi:[1,0]
	v_pk_mul_f32 v[52:53], v[52:53], v[142:143] op_sel_hi:[1,0]
	v_pk_mul_f32 v[58:59], v[58:59], v[144:145] op_sel_hi:[1,0]
	v_pk_mul_f32 v[56:57], v[56:57], v[144:145] op_sel_hi:[1,0]
	v_pk_mul_f32 v[62:63], v[62:63], v[146:147] op_sel_hi:[1,0]
	v_pk_mul_f32 v[60:61], v[60:61], v[146:147] op_sel_hi:[1,0]

.LBB0_107:
	s_andn2_b64 vcc, exec, s[8:9]
	s_cbranch_vccnz .LBB0_65
	s_ashr_i32 s0, s66, 31
	s_lshr_b32 s0, s0, 20
	s_add_i32 s0, s66, s0
	v_readlane_b32 s36, v253, 17
	s_ashr_i32 s12, s0, 12
	v_readlane_b32 s46, v253, 27
	v_readlane_b32 s47, v253, 28
	s_mov_b32 s2, s76
	s_and_b32 s14, s0, 0xfffff000
	s_ashr_i32 s13, s12, 31
	v_readlane_b32 s37, v253, 18
	v_readlane_b32 s38, v253, 19
	v_readlane_b32 s39, v253, 20
	v_readlane_b32 s40, v253, 21
	v_readlane_b32 s41, v253, 22
	v_readlane_b32 s42, v253, 23
	v_readlane_b32 s43, v253, 24
	v_readlane_b32 s44, v253, 25
	v_readlane_b32 s45, v253, 26
	s_mov_b64 s[78:79], s[46:47]
	s_sub_i32 s0, s66, s14
	s_lshl_b64 s[8:9], s[12:13], 26
	s_mov_b64 s[68:69], s[36:37]
	s_add_u32 s68, s78, s8
	s_addc_u32 s69, s79, s9
	s_ashr_i32 s8, s0, 31
	s_lshr_b32 s8, s8, 26
	s_add_i32 s8, s0, s8
	s_and_b32 s10, s8, 0xffffffc0
	s_lshl_b32 s8, s8, 6
	v_add_u32_e32 v74, s10, v77
	s_and_b32 s8, s8, 0xfffff000
	s_lshl_b32 s0, s0, 6
	v_ashrrev_i32_e32 v75, 31, v74
	s_sub_i32 s8, s0, s8
	v_lshlrev_b64 v[0:1], 14, v[74:75]
	v_lshl_add_u64 v[0:1], s[68:69], 0, v[0:1]
	s_ashr_i32 s9, s8, 31
	v_lshl_add_u64 v[0:1], s[8:9], 2, v[0:1]
	v_lshl_add_u64 v[56:57], v[0:1], 0, v[64:65]
	v_add_co_u32_e32 v4, vcc, s31, v56
	s_mov_b64 s[70:71], s[38:39]
	s_nop 0
	v_addc_co_u32_e32 v5, vcc, 0, v57, vcc
	v_add_co_u32_e32 v8, vcc, s33, v56
	global_load_dwordx4 v[0:3], v[56:57], off
	s_nop 0
	global_load_dwordx4 v[4:7], v[4:5], off
	v_addc_co_u32_e32 v9, vcc, 0, v57, vcc
	v_add_co_u32_e32 v12, vcc, s34, v56
	v_readlane_b32 s48, v253, 29
	s_nop 0
	v_addc_co_u32_e32 v13, vcc, 0, v57, vcc
	v_add_co_u32_e32 v16, vcc, s35, v56
	global_load_dwordx4 v[8:11], v[8:9], off
	s_nop 0
	global_load_dwordx4 v[12:15], v[12:13], off
	v_addc_co_u32_e32 v17, vcc, 0, v57, vcc
	v_add_co_u32_e32 v20, vcc, s52, v56
	v_readlane_b32 s49, v253, 30
	s_nop 0
	v_addc_co_u32_e32 v21, vcc, 0, v57, vcc
	v_add_co_u32_e32 v24, vcc, s53, v56
	global_load_dwordx4 v[16:19], v[16:17], off
	s_nop 0
	global_load_dwordx4 v[20:23], v[20:21], off
	v_addc_co_u32_e32 v25, vcc, 0, v57, vcc
	v_add_co_u32_e32 v28, vcc, s54, v56
	v_readlane_b32 s50, v253, 31
	s_nop 0
	v_addc_co_u32_e32 v29, vcc, 0, v57, vcc
	v_add_co_u32_e32 v32, vcc, s55, v56
	global_load_dwordx4 v[24:27], v[24:25], off
	s_nop 0
	global_load_dwordx4 v[28:31], v[28:29], off
	v_addc_co_u32_e32 v33, vcc, 0, v57, vcc
	v_add_co_u32_e32 v36, vcc, s95, v56
	v_readlane_b32 s51, v253, 32
	s_nop 0
	v_addc_co_u32_e32 v37, vcc, 0, v57, vcc
	v_add_co_u32_e32 v40, vcc, s60, v56
	global_load_dwordx4 v[32:35], v[32:33], off
	s_nop 0
	global_load_dwordx4 v[36:39], v[36:37], off
	v_addc_co_u32_e32 v41, vcc, 0, v57, vcc
	v_add_co_u32_e32 v44, vcc, s30, v56
	s_mov_b64 s[76:77], s[44:45]
	s_nop 0
	v_addc_co_u32_e32 v45, vcc, 0, v57, vcc
	v_add_co_u32_e32 v48, vcc, s59, v56
	global_load_dwordx4 v[40:43], v[40:41], off
	s_nop 0
	global_load_dwordx4 v[44:47], v[44:45], off
	v_addc_co_u32_e32 v49, vcc, 0, v57, vcc
	v_add_co_u32_e32 v52, vcc, 0xd0000, v56
	s_mov_b64 s[74:75], s[42:43]
	s_nop 0
	v_addc_co_u32_e32 v53, vcc, 0, v57, vcc
	v_add_co_u32_e32 v58, vcc, 0xe0000, v56
	global_load_dwordx4 v[48:51], v[48:49], off
	s_nop 0
	global_load_dwordx4 v[52:55], v[52:53], off
	v_addc_co_u32_e32 v59, vcc, 0, v57, vcc
	v_add_co_u32_e32 v56, vcc, 0xf0000, v56
	s_mov_b64 s[72:73], s[40:41]
	s_nop 0
	v_addc_co_u32_e32 v57, vcc, 0, v57, vcc
	global_load_dwordx4 v[60:63], v[58:59], off
	s_nop 0
	global_load_dwordx4 v[56:59], v[56:57], off
	s_andn2_b64 vcc, exec, s[62:63]
	s_cbranch_vccnz .LBB0_64
	s_ashr_i32 s15, s14, 31
	s_lshl_b64 s[14:15], s[14:15], 2
	s_add_u32 s14, s70, s14
	s_addc_u32 s15, s71, s15
	v_lshl_add_u64 v[74:75], v[74:75], 2, s[14:15]
	global_load_dword v116, v[74:75], off
	global_load_dword v118, v[74:75], off offset:16
	global_load_dword v120, v[74:75], off offset:32
	global_load_dword v122, v[74:75], off offset:48
	global_load_dword v124, v[74:75], off offset:64
	global_load_dword v126, v[74:75], off offset:80
	global_load_dword v128, v[74:75], off offset:96
	global_load_dword v130, v[74:75], off offset:112
	global_load_dword v132, v[74:75], off offset:128
	global_load_dword v134, v[74:75], off offset:144
	global_load_dword v136, v[74:75], off offset:160
	global_load_dword v138, v[74:75], off offset:176
	global_load_dword v140, v[74:75], off offset:192
	global_load_dword v142, v[74:75], off offset:208
	global_load_dword v144, v[74:75], off offset:224
	global_load_dword v146, v[74:75], off offset:240
	s_waitcnt vmcnt(0)
	v_pk_mul_f32 v[2:3], v[2:3], v[116:117] op_sel_hi:[1,0]
	v_pk_mul_f32 v[0:1], v[0:1], v[116:117] op_sel_hi:[1,0]
	v_pk_mul_f32 v[6:7], v[6:7], v[118:119] op_sel_hi:[1,0]
	v_pk_mul_f32 v[4:5], v[4:5], v[118:119] op_sel_hi:[1,0]
	v_pk_mul_f32 v[10:11], v[10:11], v[120:121] op_sel_hi:[1,0]
	v_pk_mul_f32 v[8:9], v[8:9], v[120:121] op_sel_hi:[1,0]
	v_pk_mul_f32 v[14:15], v[14:15], v[122:123] op_sel_hi:[1,0]
	v_pk_mul_f32 v[12:13], v[12:13], v[122:123] op_sel_hi:[1,0]
	v_pk_mul_f32 v[18:19], v[18:19], v[124:125] op_sel_hi:[1,0]
	v_pk_mul_f32 v[16:17], v[16:17], v[124:125] op_sel_hi:[1,0]
	v_pk_mul_f32 v[22:23], v[22:23], v[126:127] op_sel_hi:[1,0]
	v_pk_mul_f32 v[20:21], v[20:21], v[126:127] op_sel_hi:[1,0]
	v_pk_mul_f32 v[26:27], v[26:27], v[128:129] op_sel_hi:[1,0]
	v_pk_mul_f32 v[24:25], v[24:25], v[128:129] op_sel_hi:[1,0]
	v_pk_mul_f32 v[30:31], v[30:31], v[130:131] op_sel_hi:[1,0]
	v_pk_mul_f32 v[28:29], v[28:29], v[130:131] op_sel_hi:[1,0]
	v_pk_mul_f32 v[34:35], v[34:35], v[132:133] op_sel_hi:[1,0]
	v_pk_mul_f32 v[32:33], v[32:33], v[132:133] op_sel_hi:[1,0]
	v_pk_mul_f32 v[38:39], v[38:39], v[134:135] op_sel_hi:[1,0]
	v_pk_mul_f32 v[36:37], v[36:37], v[134:135] op_sel_hi:[1,0]
	v_pk_mul_f32 v[42:43], v[42:43], v[136:137] op_sel_hi:[1,0]
	v_pk_mul_f32 v[40:41], v[40:41], v[136:137] op_sel_hi:[1,0]
	v_pk_mul_f32 v[46:47], v[46:47], v[138:139] op_sel_hi:[1,0]
	v_pk_mul_f32 v[44:45], v[44:45], v[138:139] op_sel_hi:[1,0]
	v_pk_mul_f32 v[50:51], v[50:51], v[140:141] op_sel_hi:[1,0]
	v_pk_mul_f32 v[48:49], v[48:49], v[140:141] op_sel_hi:[1,0]
	v_pk_mul_f32 v[54:55], v[54:55], v[142:143] op_sel_hi:[1,0]
	v_pk_mul_f32 v[52:53], v[52:53], v[142:143] op_sel_hi:[1,0]
	v_pk_mul_f32 v[62:63], v[62:63], v[144:145] op_sel_hi:[1,0]
	v_pk_mul_f32 v[60:61], v[60:61], v[144:145] op_sel_hi:[1,0]
	v_pk_mul_f32 v[58:59], v[58:59], v[146:147] op_sel_hi:[1,0]
	v_pk_mul_f32 v[56:57], v[56:57], v[146:147] op_sel_hi:[1,0]
	s_branch .LBB0_64
